# best version plus per-gap SALU (key code s_add / s_nop) hoisted out of the MFMA gaps to the step start
# speedup vs baseline: 1.0074x; 1.0053x over previous
.LBB1_7:
	ds_read_b128 v[116:119], v181
	ds_read_b128 v[18:21], v114
	ds_read_b128 v[22:25], v114 offset:32
	ds_read_b128 v[26:29], v114 offset:64
	ds_read_b128 v[30:33], v114 offset:96
	ds_read_b128 v[120:123], v181 offset:1024
	ds_read_b128 v[124:127], v181 offset:2048
	ds_read_b128 v[128:131], v181 offset:3072
	s_add_i32 s52, s3, 0
	s_add_i32 s53, s3, 1
	s_add_i32 s54, s3, 2
	s_add_i32 s55, s3, 3
	s_add_i32 s56, s3, 4
	s_add_i32 s57, s3, 5
	s_add_i32 s58, s3, 6
	s_add_i32 s59, s3, 7
	s_add_i32 s60, s3, 8
	s_add_i32 s61, s3, 9
	s_add_i32 s62, s3, 10
	s_add_i32 s63, s3, 11
	s_add_i32 s64, s3, 12
	s_add_i32 s65, s3, 13
	s_add_i32 s66, s3, 14
	s_add_i32 s67, s3, 15
	s_add_i32 s68, s11, -32
	s_add_i32 s69, s11, -31
	s_add_i32 s70, s11, -30
	s_add_i32 s71, s11, -29
	s_add_i32 s72, s11, -28
	s_add_i32 s73, s11, -27
	s_add_i32 s74, s11, -26
	s_add_i32 s75, s11, -25
	s_add_i32 s76, s11, -24
	s_add_i32 s77, s11, -23
	s_add_i32 s78, s11, -22
	s_add_i32 s79, s11, -21
	s_add_i32 s80, s11, -20
	s_add_i32 s81, s11, -19
	s_add_i32 s82, s11, -18
	s_add_i32 s83, s11, -17
	s_waitcnt lgkmcnt(3)
	v_mfma_f32_32x32x16_f16 v[18:33], v[116:119], v[94:97], v[18:33]
	ds_read_b128 v[116:119], v181 offset:4096
	v_and_or_b32 v2, v2, v177, s52
	v_med3_f32 v115, v196, v195, v2
	v_med3_f32 v136, v197, v196, v2
	v_med3_f32 v137, v198, v197, v2
	v_med3_f32 v2, v198, v2, s42
	ds_read_b128 v[132:135], v181 offset:5120
	s_waitcnt lgkmcnt(4)
	v_mfma_f32_32x32x16_f16 v[18:33], v[120:123], v[90:93], v[18:33]
	v_and_or_b32 v3, v3, v177, s53
	v_med3_f32 v115, v136, v115, v3
	v_med3_f32 v136, v137, v136, v3
	v_med3_f32 v137, v2, v137, v3
	v_med3_f32 v2, v2, v3, s42
	ds_read_b128 v[120:123], v181 offset:6144
	s_waitcnt lgkmcnt(4)
	v_mfma_f32_32x32x16_f16 v[18:33], v[124:127], v[86:89], v[18:33]
	v_and_or_b32 v3, v4, v177, s54
	v_med3_f32 v4, v136, v115, v3
	v_med3_f32 v115, v137, v136, v3
	v_med3_f32 v136, v2, v137, v3
	v_med3_f32 v2, v2, v3, s42
	ds_read_b128 v[124:127], v181 offset:7168
	s_waitcnt lgkmcnt(4)
	v_mfma_f32_32x32x16_f16 v[18:33], v[128:131], v[82:85], v[18:33]
	v_and_or_b32 v3, v5, v177, s55
	v_med3_f32 v137, v115, v4, v3
	v_med3_f32 v115, v136, v115, v3
	v_med3_f32 v128, v2, v136, v3
	v_med3_f32 v129, v2, v3, s42
	ds_read_b128 v[2:5], v181 offset:8192
	s_waitcnt lgkmcnt(4)
	v_mfma_f32_32x32x16_f16 v[18:33], v[116:119], v[78:81], v[18:33]
	v_and_or_b32 v6, v6, v177, s56
	v_med3_f32 v130, v115, v137, v6
	v_med3_f32 v115, v128, v115, v6
	v_med3_f32 v128, v129, v128, v6
	v_med3_f32 v6, v129, v6, s42
	ds_read_b128 v[116:119], v181 offset:9216
	s_waitcnt lgkmcnt(4)
	v_mfma_f32_32x32x16_f16 v[18:33], v[132:135], v[74:77], v[18:33]
	v_and_or_b32 v7, v7, v177, s57
	v_med3_f32 v132, v6, v128, v7
	v_med3_f32 v6, v6, v7, s42
	v_med3_f32 v136, v115, v130, v7
	v_med3_f32 v115, v128, v115, v7
	ds_read_b128 v[128:131], v181 offset:10240
	s_waitcnt lgkmcnt(4)
	v_mfma_f32_32x32x16_f16 v[18:33], v[120:123], v[70:73], v[18:33]
	v_and_or_b32 v7, v8, v177, s58
	v_med3_f32 v8, v115, v136, v7
	v_med3_f32 v115, v132, v115, v7
	v_med3_f32 v132, v6, v132, v7
	v_med3_f32 v6, v6, v7, s42
	ds_read_b128 v[120:123], v181 offset:11264
	s_waitcnt lgkmcnt(4)
	v_mfma_f32_32x32x16_f16 v[18:33], v[124:127], v[66:69], v[18:33]
	v_and_or_b32 v7, v9, v177, s59
	v_med3_f32 v133, v115, v8, v7
	v_med3_f32 v115, v132, v115, v7
	v_med3_f32 v124, v6, v132, v7
	v_med3_f32 v125, v6, v7, s42
	ds_read_b128 v[6:9], v181 offset:12288
	s_waitcnt lgkmcnt(4)
	v_mfma_f32_32x32x16_f16 v[18:33], v[2:5], v[62:65], v[18:33]
	v_and_or_b32 v10, v10, v177, s60
	v_med3_f32 v126, v115, v133, v10
	v_med3_f32 v115, v124, v115, v10
	v_med3_f32 v124, v125, v124, v10
	v_med3_f32 v10, v125, v10, s42
	ds_read_b128 v[2:5], v181 offset:13312
	s_waitcnt lgkmcnt(4)
	v_mfma_f32_32x32x16_f16 v[18:33], v[116:119], v[58:61], v[18:33]
	v_and_or_b32 v11, v11, v177, s61
	v_med3_f32 v125, v115, v126, v11
	v_med3_f32 v115, v124, v115, v11
	v_med3_f32 v124, v10, v124, v11
	v_med3_f32 v10, v10, v11, s42
	ds_read_b128 v[116:119], v181 offset:14336
	s_waitcnt lgkmcnt(4)
	v_mfma_f32_32x32x16_f16 v[18:33], v[128:131], v[54:57], v[18:33]
	v_and_or_b32 v11, v12, v177, s62
	v_med3_f32 v12, v115, v125, v11
	v_med3_f32 v128, v10, v124, v11
	v_med3_f32 v10, v10, v11, s42
	v_med3_f32 v115, v124, v115, v11
	ds_read_b128 v[124:127], v181 offset:15360
	s_waitcnt lgkmcnt(4)
	v_mfma_f32_32x32x16_f16 v[18:33], v[120:123], v[50:53], v[18:33]
	v_and_or_b32 v11, v13, v177, s63
	v_med3_f32 v12, v115, v12, v11
	v_med3_f32 v13, v128, v115, v11
	v_med3_f32 v115, v10, v128, v11
	v_med3_f32 v10, v10, v11, s42
	s_waitcnt lgkmcnt(3)
	v_mfma_f32_32x32x16_f16 v[18:33], v[6:9], v[46:49], v[18:33]
	v_and_or_b32 v11, v14, v177, s64
	v_med3_f32 v12, v13, v12, v11
	v_med3_f32 v13, v115, v13, v11
	v_med3_f32 v14, v10, v115, v11
	v_med3_f32 v6, v10, v11, s42
	s_waitcnt lgkmcnt(2)
	v_mfma_f32_32x32x16_f16 v[18:33], v[2:5], v[42:45], v[18:33]
	v_and_or_b32 v7, v15, v177, s65
	v_med3_f32 v8, v13, v12, v7
	v_med3_f32 v9, v14, v13, v7
	v_med3_f32 v10, v6, v14, v7
	v_med3_f32 v2, v6, v7, s42
	s_waitcnt lgkmcnt(1)
	v_mfma_f32_32x32x16_f16 v[18:33], v[116:119], v[38:41], v[18:33]
	v_and_or_b32 v3, v16, v177, s66
	v_med3_f32 v4, v9, v8, v3
	v_med3_f32 v5, v10, v9, v3
	v_med3_f32 v6, v2, v10, v3
	v_med3_f32 v2, v2, v3, s42
	s_waitcnt lgkmcnt(0)
	v_mfma_f32_32x32x16_f16 v[18:33], v[124:127], v[34:37], v[18:33]
	v_and_or_b32 v3, v17, v177, s67
	v_med3_f32 v115, v5, v4, v3
	v_med3_f32 v132, v6, v5, v3
	v_med3_f32 v133, v2, v6, v3
	v_med3_f32 v134, v2, v3, s42
	ds_read_b128 v[116:119], v181 offset:16384
	ds_read_b128 v[2:5], v114 offset:128
	ds_read_b128 v[6:9], v114 offset:160
	ds_read_b128 v[10:13], v114 offset:192
	ds_read_b128 v[14:17], v114 offset:224
	ds_read_b128 v[120:123], v181 offset:17408
	ds_read_b128 v[124:127], v181 offset:18432
	ds_read_b128 v[128:131], v181 offset:19456
	s_sub_i32 s3, s11, 32
	s_waitcnt lgkmcnt(3)
	v_mfma_f32_32x32x16_f16 v[2:17], v[116:119], v[94:97], v[2:17]
	ds_read_b128 v[116:119], v181 offset:20480
	v_and_or_b32 v18, v18, v177, s68
	v_med3_f32 v115, v132, v115, v18
	v_med3_f32 v136, v133, v132, v18
	v_med3_f32 v137, v134, v133, v18
	v_med3_f32 v18, v134, v18, s42
	s_waitcnt lgkmcnt(3)
	v_mfma_f32_32x32x16_f16 v[2:17], v[120:123], v[90:93], v[2:17]
	ds_read_b128 v[132:135], v181 offset:21504
	v_and_or_b32 v19, v19, v177, s69
	v_med3_f32 v115, v136, v115, v19
	v_med3_f32 v136, v137, v136, v19
	v_med3_f32 v137, v18, v137, v19
	v_med3_f32 v18, v18, v19, s42
	s_waitcnt lgkmcnt(3)
	v_mfma_f32_32x32x16_f16 v[2:17], v[124:127], v[86:89], v[2:17]
	ds_read_b128 v[120:123], v181 offset:22528
	v_and_or_b32 v19, v20, v177, s70
	v_med3_f32 v20, v136, v115, v19
	v_med3_f32 v115, v137, v136, v19
	v_med3_f32 v136, v18, v137, v19
	v_med3_f32 v18, v18, v19, s42
	s_waitcnt lgkmcnt(3)
	v_mfma_f32_32x32x16_f16 v[2:17], v[128:131], v[82:85], v[2:17]
	ds_read_b128 v[124:127], v181 offset:23552
	v_and_or_b32 v19, v21, v177, s71
	v_med3_f32 v137, v115, v20, v19
	v_med3_f32 v115, v136, v115, v19
	v_med3_f32 v128, v18, v136, v19
	v_med3_f32 v129, v18, v19, s42
	s_waitcnt lgkmcnt(3)
	v_mfma_f32_32x32x16_f16 v[2:17], v[116:119], v[78:81], v[2:17]
	ds_read_b128 v[18:21], v181 offset:24576
	v_and_or_b32 v22, v22, v177, s72
	v_med3_f32 v130, v115, v137, v22
	v_med3_f32 v115, v128, v115, v22
	v_med3_f32 v128, v129, v128, v22
	v_med3_f32 v22, v129, v22, s42
	s_waitcnt lgkmcnt(3)
	v_mfma_f32_32x32x16_f16 v[2:17], v[132:135], v[74:77], v[2:17]
	ds_read_b128 v[116:119], v181 offset:25600
	v_and_or_b32 v23, v23, v177, s73
	v_med3_f32 v136, v115, v130, v23
	v_med3_f32 v115, v128, v115, v23
	v_med3_f32 v132, v22, v128, v23
	v_med3_f32 v22, v22, v23, s42
	s_waitcnt lgkmcnt(3)
	v_mfma_f32_32x32x16_f16 v[2:17], v[120:123], v[70:73], v[2:17]
	ds_read_b128 v[128:131], v181 offset:26624
	v_and_or_b32 v23, v24, v177, s74
	v_med3_f32 v24, v115, v136, v23
	v_med3_f32 v115, v132, v115, v23
	v_med3_f32 v132, v22, v132, v23
	v_med3_f32 v22, v22, v23, s42
	s_waitcnt lgkmcnt(3)
	v_mfma_f32_32x32x16_f16 v[2:17], v[124:127], v[66:69], v[2:17]
	ds_read_b128 v[120:123], v181 offset:27648
	v_and_or_b32 v23, v25, v177, s75
	v_med3_f32 v133, v115, v24, v23
	v_med3_f32 v115, v132, v115, v23
	v_med3_f32 v124, v22, v132, v23
	v_med3_f32 v125, v22, v23, s42
	s_waitcnt lgkmcnt(3)
	v_mfma_f32_32x32x16_f16 v[2:17], v[18:21], v[62:65], v[2:17]
	ds_read_b128 v[22:25], v181 offset:28672
	v_and_or_b32 v26, v26, v177, s76
	v_med3_f32 v126, v115, v133, v26
	v_med3_f32 v115, v124, v115, v26
	v_med3_f32 v124, v125, v124, v26
	v_med3_f32 v26, v125, v26, s42
	s_waitcnt lgkmcnt(3)
	v_mfma_f32_32x32x16_f16 v[2:17], v[116:119], v[58:61], v[2:17]
	ds_read_b128 v[18:21], v181 offset:29696
	v_and_or_b32 v27, v27, v177, s77
	v_med3_f32 v125, v115, v126, v27
	v_med3_f32 v115, v124, v115, v27
	v_med3_f32 v124, v26, v124, v27
	v_med3_f32 v26, v26, v27, s42
	s_waitcnt lgkmcnt(3)
	v_mfma_f32_32x32x16_f16 v[2:17], v[128:131], v[54:57], v[2:17]
	ds_read_b128 v[116:119], v181 offset:30720
	v_and_or_b32 v27, v28, v177, s78
	v_med3_f32 v28, v115, v125, v27
	v_med3_f32 v115, v124, v115, v27
	v_med3_f32 v128, v26, v124, v27
	v_med3_f32 v26, v26, v27, s42
	s_waitcnt lgkmcnt(3)
	v_mfma_f32_32x32x16_f16 v[2:17], v[120:123], v[50:53], v[2:17]
	ds_read_b128 v[124:127], v181 offset:31744
	v_and_or_b32 v27, v29, v177, s79
	v_med3_f32 v28, v115, v28, v27
	v_med3_f32 v29, v128, v115, v27
	v_med3_f32 v115, v26, v128, v27
	v_med3_f32 v26, v26, v27, s42
	s_waitcnt lgkmcnt(3)
	v_mfma_f32_32x32x16_f16 v[2:17], v[22:25], v[46:49], v[2:17]
	v_and_or_b32 v27, v30, v177, s80
	v_med3_f32 v28, v29, v28, v27
	v_med3_f32 v29, v115, v29, v27
	v_med3_f32 v30, v26, v115, v27
	v_med3_f32 v22, v26, v27, s42
	s_waitcnt lgkmcnt(2)
	v_mfma_f32_32x32x16_f16 v[2:17], v[18:21], v[42:45], v[2:17]
	v_and_or_b32 v23, v31, v177, s81
	v_med3_f32 v24, v29, v28, v23
	v_med3_f32 v25, v30, v29, v23
	v_med3_f32 v26, v22, v30, v23
	v_med3_f32 v18, v22, v23, s42
	s_waitcnt lgkmcnt(1)
	v_mfma_f32_32x32x16_f16 v[2:17], v[116:119], v[38:41], v[2:17]
	v_and_or_b32 v19, v32, v177, s82
	v_med3_f32 v20, v25, v24, v19
	v_med3_f32 v21, v26, v25, v19
	v_med3_f32 v22, v18, v26, v19
	v_med3_f32 v18, v18, v19, s42
	s_waitcnt lgkmcnt(0)
	v_mfma_f32_32x32x16_f16 v[2:17], v[124:127], v[34:37], v[2:17]
	v_and_or_b32 v19, v33, v177, s83
	v_med3_f32 v115, v21, v20, v19
	v_med3_f32 v132, v22, v21, v19
	v_med3_f32 v133, v18, v22, v19
	v_med3_f32 v134, v18, v19, s42
	s_barrier
	ds_read_b128 v[116:119], v181 offset:32768
	ds_read_b128 v[18:21], v114 offset:256
	ds_read_b128 v[22:25], v114 offset:288
	ds_read_b128 v[26:29], v114 offset:320
	ds_read_b128 v[30:33], v114 offset:352
	ds_read_b128 v[120:123], v181 offset:33792
	ds_read_b128 v[124:127], v181 offset:34816
	ds_read_b128 v[128:131], v181 offset:35840
	s_add_i32 s3, s11, -16
	s_add_i32 s52, s11, -16
	s_add_i32 s53, s11, -15
	s_add_i32 s54, s11, -14
	s_add_i32 s55, s11, -13
	s_add_i32 s56, s11, -12
	s_add_i32 s57, s11, -11
	s_add_i32 s58, s11, -10
	s_add_i32 s59, s11, -9
	s_add_i32 s60, s11, -8
	s_add_i32 s61, s11, -7
	s_add_i32 s62, s11, -6
	s_add_i32 s63, s11, -5
	s_add_i32 s64, s11, -4
	s_add_i32 s65, s11, -3
	s_add_i32 s66, s11, -2
	s_add_i32 s67, s11, -1
	s_add_i32 s68, s11, 0
	s_add_i32 s69, s11, 1
	s_add_i32 s70, s11, 2
	s_add_i32 s71, s11, 3
	s_add_i32 s72, s11, 4
	s_add_i32 s73, s11, 5
	s_add_i32 s74, s11, 6
	s_add_i32 s75, s11, 7
	s_add_i32 s76, s11, 8
	s_add_i32 s77, s11, 9
	s_add_i32 s78, s11, 10
	s_add_i32 s79, s11, 11
	s_add_i32 s80, s11, 12
	s_add_i32 s81, s11, 13
	s_add_i32 s82, s11, 14
	s_add_i32 s83, s11, 15
	s_waitcnt lgkmcnt(3)
	v_mfma_f32_32x32x16_f16 v[18:33], v[116:119], v[94:97], v[18:33]
	ds_read_b128 v[116:119], v181 offset:36864
	v_and_or_b32 v2, v2, v177, s52
	v_med3_f32 v115, v132, v115, v2
	v_med3_f32 v136, v133, v132, v2
	v_med3_f32 v137, v134, v133, v2
	v_med3_f32 v2, v134, v2, s42
	ds_read_b128 v[132:135], v181 offset:37888
	s_waitcnt lgkmcnt(4)
	v_mfma_f32_32x32x16_f16 v[18:33], v[120:123], v[90:93], v[18:33]
	v_and_or_b32 v3, v3, v177, s53
	v_med3_f32 v115, v136, v115, v3
	v_med3_f32 v136, v137, v136, v3
	v_med3_f32 v137, v2, v137, v3
	v_med3_f32 v2, v2, v3, s42
	ds_read_b128 v[120:123], v181 offset:38912
	s_waitcnt lgkmcnt(4)
	v_mfma_f32_32x32x16_f16 v[18:33], v[124:127], v[86:89], v[18:33]
	v_and_or_b32 v3, v4, v177, s54
	v_med3_f32 v4, v136, v115, v3
	v_med3_f32 v115, v137, v136, v3
	v_med3_f32 v136, v2, v137, v3
	v_med3_f32 v2, v2, v3, s42
	ds_read_b128 v[124:127], v181 offset:39936
	s_waitcnt lgkmcnt(4)
	v_mfma_f32_32x32x16_f16 v[18:33], v[128:131], v[82:85], v[18:33]
	v_and_or_b32 v3, v5, v177, s55
	v_med3_f32 v137, v115, v4, v3
	v_med3_f32 v115, v136, v115, v3
	v_med3_f32 v128, v2, v136, v3
	v_med3_f32 v129, v2, v3, s42
	ds_read_b128 v[2:5], v181 offset:40960
	s_waitcnt lgkmcnt(4)
	v_mfma_f32_32x32x16_f16 v[18:33], v[116:119], v[78:81], v[18:33]
	v_and_or_b32 v6, v6, v177, s56
	v_med3_f32 v130, v115, v137, v6
	v_med3_f32 v115, v128, v115, v6
	v_med3_f32 v128, v129, v128, v6
	v_med3_f32 v6, v129, v6, s42
	ds_read_b128 v[116:119], v181 offset:41984
	s_waitcnt lgkmcnt(4)
	v_mfma_f32_32x32x16_f16 v[18:33], v[132:135], v[74:77], v[18:33]
	v_and_or_b32 v7, v7, v177, s57
	v_med3_f32 v132, v6, v128, v7
	v_med3_f32 v6, v6, v7, s42
	v_med3_f32 v136, v115, v130, v7
	v_med3_f32 v115, v128, v115, v7
	ds_read_b128 v[128:131], v181 offset:43008
	s_waitcnt lgkmcnt(4)
	v_mfma_f32_32x32x16_f16 v[18:33], v[120:123], v[70:73], v[18:33]
	v_and_or_b32 v7, v8, v177, s58
	v_med3_f32 v8, v115, v136, v7
	v_med3_f32 v115, v132, v115, v7
	v_med3_f32 v132, v6, v132, v7
	v_med3_f32 v6, v6, v7, s42
	ds_read_b128 v[120:123], v181 offset:44032
	s_waitcnt lgkmcnt(4)
	v_mfma_f32_32x32x16_f16 v[18:33], v[124:127], v[66:69], v[18:33]
	v_and_or_b32 v7, v9, v177, s59
	v_med3_f32 v133, v115, v8, v7
	v_med3_f32 v115, v132, v115, v7
	v_med3_f32 v124, v6, v132, v7
	v_med3_f32 v125, v6, v7, s42
	ds_read_b128 v[6:9], v181 offset:45056
	s_waitcnt lgkmcnt(4)
	v_mfma_f32_32x32x16_f16 v[18:33], v[2:5], v[62:65], v[18:33]
	v_and_or_b32 v10, v10, v177, s60
	v_med3_f32 v126, v115, v133, v10
	v_med3_f32 v115, v124, v115, v10
	v_med3_f32 v124, v125, v124, v10
	v_med3_f32 v10, v125, v10, s42
	ds_read_b128 v[2:5], v181 offset:46080
	s_waitcnt lgkmcnt(4)
	v_mfma_f32_32x32x16_f16 v[18:33], v[116:119], v[58:61], v[18:33]
	v_and_or_b32 v11, v11, v177, s61
	v_med3_f32 v125, v115, v126, v11
	v_med3_f32 v115, v124, v115, v11
	v_med3_f32 v124, v10, v124, v11
	v_med3_f32 v10, v10, v11, s42
	ds_read_b128 v[116:119], v181 offset:47104
	s_waitcnt lgkmcnt(4)
	v_mfma_f32_32x32x16_f16 v[18:33], v[128:131], v[54:57], v[18:33]
	v_and_or_b32 v11, v12, v177, s62
	v_med3_f32 v12, v115, v125, v11
	v_med3_f32 v128, v10, v124, v11
	v_med3_f32 v10, v10, v11, s42
	v_med3_f32 v115, v124, v115, v11
	ds_read_b128 v[124:127], v181 offset:48128
	s_waitcnt lgkmcnt(4)
	v_mfma_f32_32x32x16_f16 v[18:33], v[120:123], v[50:53], v[18:33]
	v_and_or_b32 v11, v13, v177, s63
	v_med3_f32 v12, v115, v12, v11
	v_med3_f32 v13, v128, v115, v11
	v_med3_f32 v115, v10, v128, v11
	v_med3_f32 v10, v10, v11, s42
	s_waitcnt lgkmcnt(3)
	v_mfma_f32_32x32x16_f16 v[18:33], v[6:9], v[46:49], v[18:33]
	v_and_or_b32 v11, v14, v177, s64
	v_med3_f32 v12, v13, v12, v11
	v_med3_f32 v13, v115, v13, v11
	v_med3_f32 v14, v10, v115, v11
	v_med3_f32 v6, v10, v11, s42
	s_waitcnt lgkmcnt(2)
	v_mfma_f32_32x32x16_f16 v[18:33], v[2:5], v[42:45], v[18:33]
	v_and_or_b32 v7, v15, v177, s65
	v_med3_f32 v8, v13, v12, v7
	v_med3_f32 v9, v14, v13, v7
	v_med3_f32 v10, v6, v14, v7
	v_med3_f32 v2, v6, v7, s42
	s_waitcnt lgkmcnt(1)
	v_mfma_f32_32x32x16_f16 v[18:33], v[116:119], v[38:41], v[18:33]
	v_and_or_b32 v3, v16, v177, s66
	v_med3_f32 v4, v9, v8, v3
	v_med3_f32 v5, v10, v9, v3
	v_med3_f32 v6, v2, v10, v3
	v_med3_f32 v2, v2, v3, s42
	s_waitcnt lgkmcnt(0)
	v_mfma_f32_32x32x16_f16 v[18:33], v[124:127], v[34:37], v[18:33]
	v_and_or_b32 v3, v17, v177, s67
	v_med3_f32 v115, v5, v4, v3
	v_med3_f32 v132, v6, v5, v3
	v_med3_f32 v133, v2, v6, v3
	v_med3_f32 v134, v2, v3, s42
	ds_read_b128 v[116:119], v181 offset:49152
	ds_read_b128 v[2:5], v114 offset:384
	ds_read_b128 v[6:9], v114 offset:416
	ds_read_b128 v[10:13], v114 offset:448
	ds_read_b128 v[14:17], v114 offset:480
	ds_read_b128 v[120:123], v181 offset:50176
	ds_read_b128 v[124:127], v181 offset:51200
	ds_read_b128 v[128:131], v181 offset:52224
	s_mov_b32 s3, s11
	s_waitcnt lgkmcnt(3)
	v_mfma_f32_32x32x16_f16 v[2:17], v[116:119], v[94:97], v[2:17]
	ds_read_b128 v[116:119], v181 offset:53248
	v_and_or_b32 v18, v18, v177, s68
	v_med3_f32 v115, v132, v115, v18
	v_med3_f32 v136, v133, v132, v18
	v_med3_f32 v137, v134, v133, v18
	v_med3_f32 v18, v134, v18, s42
	s_waitcnt lgkmcnt(3)
	v_mfma_f32_32x32x16_f16 v[2:17], v[120:123], v[90:93], v[2:17]
	ds_read_b128 v[132:135], v181 offset:54272
	v_and_or_b32 v19, v19, v177, s69
	v_med3_f32 v115, v136, v115, v19
	v_med3_f32 v136, v137, v136, v19
	v_med3_f32 v137, v18, v137, v19
	v_med3_f32 v18, v18, v19, s42
	s_waitcnt lgkmcnt(3)
	v_mfma_f32_32x32x16_f16 v[2:17], v[124:127], v[86:89], v[2:17]
	ds_read_b128 v[120:123], v181 offset:55296
	v_and_or_b32 v19, v20, v177, s70
	v_med3_f32 v20, v136, v115, v19
	v_med3_f32 v115, v137, v136, v19
	v_med3_f32 v136, v18, v137, v19
	v_med3_f32 v18, v18, v19, s42
	s_waitcnt lgkmcnt(3)
	v_mfma_f32_32x32x16_f16 v[2:17], v[128:131], v[82:85], v[2:17]
	ds_read_b128 v[124:127], v181 offset:56320
	v_and_or_b32 v19, v21, v177, s71
	v_med3_f32 v137, v115, v20, v19
	v_med3_f32 v115, v136, v115, v19
	v_med3_f32 v128, v18, v136, v19
	v_med3_f32 v129, v18, v19, s42
	s_waitcnt lgkmcnt(3)
	v_mfma_f32_32x32x16_f16 v[2:17], v[116:119], v[78:81], v[2:17]
	ds_read_b128 v[18:21], v181 offset:57344
	v_and_or_b32 v22, v22, v177, s72
	v_med3_f32 v130, v115, v137, v22
	v_med3_f32 v115, v128, v115, v22
	v_med3_f32 v128, v129, v128, v22
	v_med3_f32 v22, v129, v22, s42
	s_waitcnt lgkmcnt(3)
	v_mfma_f32_32x32x16_f16 v[2:17], v[132:135], v[74:77], v[2:17]
	ds_read_b128 v[116:119], v181 offset:58368
	v_and_or_b32 v23, v23, v177, s73
	v_med3_f32 v136, v115, v130, v23
	v_med3_f32 v115, v128, v115, v23
	v_med3_f32 v132, v22, v128, v23
	v_med3_f32 v22, v22, v23, s42
	s_waitcnt lgkmcnt(3)
	v_mfma_f32_32x32x16_f16 v[2:17], v[120:123], v[70:73], v[2:17]
	ds_read_b128 v[128:131], v181 offset:59392
	v_and_or_b32 v23, v24, v177, s74
	v_med3_f32 v24, v115, v136, v23
	v_med3_f32 v115, v132, v115, v23
	v_med3_f32 v132, v22, v132, v23
	v_med3_f32 v22, v22, v23, s42
	s_waitcnt lgkmcnt(3)
	v_mfma_f32_32x32x16_f16 v[2:17], v[124:127], v[66:69], v[2:17]
	ds_read_b128 v[120:123], v181 offset:60416
	v_and_or_b32 v23, v25, v177, s75
	v_med3_f32 v133, v115, v24, v23
	v_med3_f32 v115, v132, v115, v23
	v_med3_f32 v124, v22, v132, v23
	v_med3_f32 v125, v22, v23, s42
	s_waitcnt lgkmcnt(3)
	v_mfma_f32_32x32x16_f16 v[2:17], v[18:21], v[62:65], v[2:17]
	ds_read_b128 v[22:25], v181 offset:61440
	v_and_or_b32 v26, v26, v177, s76
	v_med3_f32 v126, v115, v133, v26
	v_med3_f32 v115, v124, v115, v26
	v_med3_f32 v124, v125, v124, v26
	v_med3_f32 v26, v125, v26, s42
	s_waitcnt lgkmcnt(3)
	v_mfma_f32_32x32x16_f16 v[2:17], v[116:119], v[58:61], v[2:17]
	ds_read_b128 v[18:21], v181 offset:62464
	v_and_or_b32 v27, v27, v177, s77
	v_med3_f32 v125, v115, v126, v27
	v_med3_f32 v115, v124, v115, v27
	v_med3_f32 v124, v26, v124, v27
	v_med3_f32 v26, v26, v27, s42
	s_waitcnt lgkmcnt(3)
	v_mfma_f32_32x32x16_f16 v[2:17], v[128:131], v[54:57], v[2:17]
	ds_read_b128 v[116:119], v181 offset:63488
	v_and_or_b32 v27, v28, v177, s78
	v_med3_f32 v28, v115, v125, v27
	v_med3_f32 v115, v124, v115, v27
	v_med3_f32 v128, v26, v124, v27
	v_med3_f32 v26, v26, v27, s42
	s_waitcnt lgkmcnt(3)
	v_mfma_f32_32x32x16_f16 v[2:17], v[120:123], v[50:53], v[2:17]
	ds_read_b128 v[124:127], v181 offset:64512
	v_and_or_b32 v27, v29, v177, s79
	v_med3_f32 v28, v115, v28, v27
	v_med3_f32 v29, v128, v115, v27
	v_med3_f32 v115, v26, v128, v27
	v_med3_f32 v26, v26, v27, s42
	s_waitcnt lgkmcnt(3)
	v_mfma_f32_32x32x16_f16 v[2:17], v[22:25], v[46:49], v[2:17]
	v_and_or_b32 v27, v30, v177, s80
	v_med3_f32 v28, v29, v28, v27
	v_med3_f32 v29, v115, v29, v27
	v_med3_f32 v30, v26, v115, v27
	v_med3_f32 v22, v26, v27, s42
	s_waitcnt lgkmcnt(2)
	v_mfma_f32_32x32x16_f16 v[2:17], v[18:21], v[42:45], v[2:17]
	v_and_or_b32 v23, v31, v177, s81
	v_med3_f32 v24, v29, v28, v23
	v_med3_f32 v25, v30, v29, v23
	v_med3_f32 v26, v22, v30, v23
	v_med3_f32 v18, v22, v23, s42
	s_waitcnt lgkmcnt(1)
	v_mfma_f32_32x32x16_f16 v[2:17], v[116:119], v[38:41], v[2:17]
	v_and_or_b32 v19, v32, v177, s82
	v_med3_f32 v20, v25, v24, v19
	v_med3_f32 v21, v26, v25, v19
	v_med3_f32 v22, v18, v26, v19
	v_med3_f32 v18, v18, v19, s42
	s_waitcnt lgkmcnt(0)
	v_mfma_f32_32x32x16_f16 v[2:17], v[124:127], v[34:37], v[2:17]
	v_and_or_b32 v19, v33, v177, s83
	v_med3_f32 v195, v21, v20, v19
	v_med3_f32 v196, v22, v21, v19
	v_med3_f32 v197, v18, v22, v19
	v_med3_f32 v198, v18, v19, s42
	s_add_i32 s3, s11, 16
	s_add_i32 s10, s10, 2
	s_add_i32 s11, s11, 64
	s_cmp_gt_u32 s10, 5
	v_add_u32_e32 v114, 0x200, v114
	s_barrier
	s_cbranch_scc0 .LBB1_7
	s_cmp_lg_u32 s40, 3
	v_and_b32_e32 v200, v2, v177
	v_and_b32_e32 v199, v3, v177
	v_and_b32_e32 v4, v4, v177
	s_mov_b64 s[10:11], -1
	s_cbranch_scc0 .LBB1_38
	s_movk_i32 s3, 0xf0
	v_cmp_gt_f32_e32 vcc, s41, v178
	v_or_b32_e32 v2, s3, v200
	s_movk_i32 s3, 0xf1
	v_med3_f32 v3, v196, v195, v2
	v_or_b32_e32 v20, s3, v199
	s_movk_i32 s3, 0xf2
	v_med3_f32 v18, v197, v196, v2
	v_med3_f32 v19, v198, v197, v2
	v_med3_f32 v2, v198, v2, s42
	v_med3_f32 v3, v18, v3, v20
	v_med3_f32 v18, v19, v18, v20
	v_med3_f32 v19, v2, v19, v20
	v_med3_f32 v2, v2, v20, s42
	v_or_b32_e32 v20, s3, v4
	s_movk_i32 s3, 0xf3
	v_med3_f32 v3, v18, v3, v20
	v_med3_f32 v18, v19, v18, v20
	v_med3_f32 v19, v2, v19, v20
	v_med3_f32 v2, v2, v20, s42
	v_and_or_b32 v20, v5, v177, s3
	s_movk_i32 s3, 0xf4
	v_med3_f32 v3, v18, v3, v20
	v_med3_f32 v18, v19, v18, v20
	v_med3_f32 v19, v2, v19, v20
	v_med3_f32 v2, v2, v20, s42
	v_and_or_b32 v20, v6, v177, s3
	s_movk_i32 s3, 0xf5
	v_med3_f32 v3, v18, v3, v20
	v_med3_f32 v18, v19, v18, v20
	v_med3_f32 v19, v2, v19, v20
	v_med3_f32 v2, v2, v20, s42
	v_and_or_b32 v20, v7, v177, s3
	s_movk_i32 s3, 0xf6
	v_med3_f32 v3, v18, v3, v20
	v_med3_f32 v18, v19, v18, v20
	v_med3_f32 v19, v2, v19, v20
	v_med3_f32 v2, v2, v20, s42
	v_and_or_b32 v20, v8, v177, s3
	s_movk_i32 s3, 0xf7
	v_med3_f32 v3, v18, v3, v20
	v_med3_f32 v18, v19, v18, v20
	v_med3_f32 v19, v2, v19, v20
	v_med3_f32 v2, v2, v20, s42
	v_and_or_b32 v20, v9, v177, s3
	s_movk_i32 s3, 0xf8
	v_med3_f32 v3, v18, v3, v20
	v_med3_f32 v18, v19, v18, v20
	v_med3_f32 v19, v2, v19, v20
	v_med3_f32 v2, v2, v20, s42
	v_and_or_b32 v20, v10, v177, s3
	s_movk_i32 s3, 0xf9
	v_med3_f32 v3, v18, v3, v20
	v_med3_f32 v18, v19, v18, v20
	v_med3_f32 v19, v2, v19, v20
	v_med3_f32 v2, v2, v20, s42
	v_and_or_b32 v20, v11, v177, s3
	s_movk_i32 s3, 0xfa
	v_med3_f32 v3, v18, v3, v20
	v_med3_f32 v18, v19, v18, v20
	v_med3_f32 v19, v2, v19, v20
	v_med3_f32 v2, v2, v20, s42
	v_and_or_b32 v20, v12, v177, s3
	s_movk_i32 s3, 0xfb
	v_med3_f32 v3, v18, v3, v20
	v_med3_f32 v18, v19, v18, v20
	v_med3_f32 v19, v2, v19, v20
	v_med3_f32 v2, v2, v20, s42
	v_and_or_b32 v20, v13, v177, s3
	s_movk_i32 s3, 0xfc
	v_med3_f32 v3, v18, v3, v20
	v_med3_f32 v18, v19, v18, v20
	v_med3_f32 v19, v2, v19, v20
	v_med3_f32 v2, v2, v20, s42
	v_and_or_b32 v20, v14, v177, s3
	s_movk_i32 s3, 0xfd
	v_med3_f32 v3, v18, v3, v20
	v_med3_f32 v18, v19, v18, v20
	v_med3_f32 v19, v2, v19, v20
	v_med3_f32 v2, v2, v20, s42
	v_and_or_b32 v20, v15, v177, s3
	s_movk_i32 s3, 0xfe
	v_med3_f32 v3, v18, v3, v20
	v_med3_f32 v18, v19, v18, v20
	v_med3_f32 v19, v2, v19, v20
	v_med3_f32 v2, v2, v20, s42
	v_and_or_b32 v20, v16, v177, s3
	s_movk_i32 s3, 0xff
	v_med3_f32 v3, v18, v3, v20
	v_med3_f32 v18, v19, v18, v20
	v_med3_f32 v19, v2, v19, v20
	v_med3_f32 v2, v2, v20, s42
	s_nop 0
	v_and_or_b32 v20, v17, v177, s3
	v_med3_f32 v3, v18, v3, v20
	v_med3_f32 v18, v19, v18, v20
	v_med3_f32 v19, v2, v19, v20
	v_med3_f32 v2, v2, v20, s42
	v_lshlrev_b32_e32 v20, 1, v2
	v_and_b32_e32 v20, 0x1f8, v20
	v_and_b32_e32 v2, 0xfffffe03, v2
	v_or3_b32 v2, v2, v20, v184
	v_lshlrev_b32_e32 v20, 1, v19
	v_and_b32_e32 v20, 0x1f8, v20
	v_and_b32_e32 v19, 0xfffffe03, v19
	v_or3_b32 v25, v19, v20, v184
	v_lshlrev_b32_e32 v19, 1, v18
	v_and_b32_e32 v19, 0x1f8, v19
	v_and_b32_e32 v18, 0xfffffe03, v18
	v_or3_b32 v18, v18, v19, v184
	v_lshlrev_b32_e32 v19, 1, v3
	v_and_b32_e32 v20, 0x1f8, v19
	ds_bpermute_b32 v19, v1, v2
	ds_bpermute_b32 v21, v1, v25
	ds_bpermute_b32 v22, v1, v18
	v_and_b32_e32 v3, 0xfffffe03, v3
	v_or3_b32 v20, v3, v20, v184
	s_waitcnt lgkmcnt(2)
	v_med3_f32 v24, v25, v18, v19
	v_med3_f32 v3, v2, v25, v19
	v_med3_f32 v2, v2, v19, s42
	s_waitcnt lgkmcnt(1)
	v_med3_f32 v25, v3, v24, v21
	v_med3_f32 v3, v2, v3, v21
	v_med3_f32 v2, v2, v21, s42
	s_waitcnt lgkmcnt(0)
	v_med3_f32 v27, v3, v25, v22
	v_med3_f32 v3, v2, v3, v22
	v_med3_f32 v26, v2, v22, s42
	v_mul_f32_e32 v2, 0x4f800000, v178
	v_cndmask_b32_e32 v28, v178, v2, vcc
	v_sqrt_f32_e32 v29, v28
	ds_bpermute_b32 v23, v1, v20
	v_add_u32_e32 v30, -1, v29
	v_fma_f32 v31, -v30, v29, v28
	v_cmp_ge_f32_e64 s[10:11], 0, v31
	v_add_u32_e32 v31, 1, v29
	s_waitcnt lgkmcnt(0)
	v_med3_f32 v2, v3, v27, v23
	v_cndmask_b32_e64 v30, v29, v30, s[10:11]
	v_fma_f32 v29, -v31, v29, v28
	v_cmp_lt_f32_e64 s[10:11], 0, v29
	v_med3_f32 v3, v26, v3, v23
	v_med3_f32 v26, v26, v23, s42
	v_cndmask_b32_e64 v29, v30, v31, s[10:11]
	v_mul_f32_e32 v30, 0x37800000, v29
	v_cndmask_b32_e32 v29, v29, v30, vcc
	v_cmp_class_f32_e32 vcc, v28, v179
	s_nop 1
	v_cndmask_b32_e32 v28, v29, v28, vcc
	v_mul_f32_e32 v28, v180, v28
	v_and_b32_e32 v29, 0x7fffffff, v26
	v_pk_mul_f32 v[28:29], v[28:29], s[24:25]
	s_nop 0
	v_add_f32_e32 v28, v28, v29
	v_sub_f32_e32 v29, v3, v26
	v_cmp_ngt_f32_e32 vcc, v29, v28
	v_mov_b32_e32 v29, 0
	s_and_saveexec_b64 s[10:11], vcc
	s_cbranch_execz .LBB1_13
	v_sub_f32_e32 v29, v2, v26
	v_cmp_ngt_f32_e32 vcc, v29, v28
	v_mov_b32_e32 v29, 1
	s_and_saveexec_b64 s[28:29], vcc
	v_med3_f32 v18, v18, v20, v19
	v_med3_f32 v18, v24, v18, v21
	v_med3_f32 v18, v25, v18, v22
	v_med3_f32 v18, v27, v18, v23
	v_sub_f32_e32 v18, v18, v26
	v_cmp_gt_f32_e32 vcc, v18, v28
	s_nop 1
	v_cndmask_b32_e64 v29, 3, 2, vcc
	s_or_b64 exec, exec, s[28:29]
